# v111 with a tighter spin interval in the down-phase dependency poll (s_sleep 8 to s_sleep 2)
# speedup vs baseline: 1.0006x; 1.0006x over previous
; __device__ __forceinline__ void phase_moe_down(const Ptrs& p, LAS unsigned char* lds) {
;     ...
;             if (threadIdx.x == 0) {
;                 unsigned* tot = (unsigned*)(p.ws + OFF_GUTOT); unsigned* de = (unsigned*)(p.ws + OFF_GUDONE) + mu.e * 16;
;                 const unsigned need = (unsigned)(((mu.cnt + 255) >> 8) * 16); int all = 0;
;                 for (unsigned sp = 0; sp < (1u << 22); ++sp) {
;                     if (__hip_atomic_load(tot, __ATOMIC_RELAXED, __HIP_MEMORY_SCOPE_AGENT) >= (unsigned)Ugu) { all = 1; break; }
;                     if (__hip_atomic_load(de, __ATOMIC_RELAXED, __HIP_MEMORY_SCOPE_AGENT) >= need) break;
;                     __builtin_amdgcn_s_sleep(8); }
;                 __builtin_amdgcn_fence(__ATOMIC_ACQUIRE, "agent");
;                 *wslot = all; }
.LBB0_1455:
	global_load_dword v3, v2, s[30:31] offset:1024 sc1
	s_waitcnt vmcnt(0)
	v_cmp_le_u32_e32 vcc, s21, v3
	s_cbranch_vccnz .LBB0_1473
	global_load_dword v3, v2, s[4:5] offset:2048 sc1
	s_waitcnt vmcnt(0)
	v_cmp_gt_u32_e32 vcc, s2, v3
	s_cbranch_vccz .LBB0_1474
	s_sleep 2
	global_load_dword v3, v2, s[30:31] offset:1024 sc1
	s_waitcnt vmcnt(0)
	v_cmp_gt_u32_e32 vcc, s21, v3
	s_cbranch_vccz .LBB0_1473
	global_load_dword v3, v2, s[4:5] offset:2048 sc1
	s_waitcnt vmcnt(0)
	v_cmp_gt_u32_e32 vcc, s2, v3
	s_cbranch_vccz .LBB0_1474
	s_sleep 2
	global_load_dword v3, v2, s[30:31] offset:1024 sc1
	s_waitcnt vmcnt(0)
	v_cmp_gt_u32_e32 vcc, s21, v3
	s_cbranch_vccz .LBB0_1473
	global_load_dword v3, v2, s[4:5] offset:2048 sc1
	s_waitcnt vmcnt(0)
	v_cmp_gt_u32_e32 vcc, s2, v3
	s_cbranch_vccz .LBB0_1474
	s_sleep 2
	global_load_dword v3, v2, s[30:31] offset:1024 sc1
	s_waitcnt vmcnt(0)
	v_cmp_gt_u32_e32 vcc, s21, v3
	s_cbranch_vccz .LBB0_1473
	global_load_dword v3, v2, s[4:5] offset:2048 sc1
	s_waitcnt vmcnt(0)
	v_cmp_gt_u32_e32 vcc, s2, v3
	s_cbranch_vccz .LBB0_1474
	s_sleep 2
	global_load_dword v3, v2, s[30:31] offset:1024 sc1
	s_waitcnt vmcnt(0)
	v_cmp_gt_u32_e32 vcc, s21, v3
	s_cbranch_vccz .LBB0_1473
	global_load_dword v3, v2, s[4:5] offset:2048 sc1
	s_waitcnt vmcnt(0)
	v_cmp_gt_u32_e32 vcc, s2, v3
	s_cbranch_vccz .LBB0_1474
	s_sleep 2
	global_load_dword v3, v2, s[30:31] offset:1024 sc1
	s_waitcnt vmcnt(0)
	v_cmp_gt_u32_e32 vcc, s21, v3
	s_cbranch_vccz .LBB0_1473
	global_load_dword v3, v2, s[4:5] offset:2048 sc1
	s_waitcnt vmcnt(0)
	v_cmp_gt_u32_e32 vcc, s2, v3
	s_cbranch_vccz .LBB0_1474
	s_sleep 2
	global_load_dword v3, v2, s[30:31] offset:1024 sc1
	s_waitcnt vmcnt(0)
	v_cmp_gt_u32_e32 vcc, s21, v3
	s_cbranch_vccz .LBB0_1473
	global_load_dword v3, v2, s[4:5] offset:2048 sc1
	s_waitcnt vmcnt(0)
	v_cmp_gt_u32_e32 vcc, s2, v3
	s_cbranch_vccz .LBB0_1474
	s_sleep 2
	global_load_dword v3, v2, s[30:31] offset:1024 sc1
	s_waitcnt vmcnt(0)
	v_cmp_gt_u32_e32 vcc, s21, v3
	s_cbranch_vccz .LBB0_1473
	global_load_dword v3, v2, s[4:5] offset:2048 sc1
	s_mov_b64 s[6:7], -1
	s_waitcnt vmcnt(0)
	v_cmp_gt_u32_e32 vcc, s2, v3
	s_cbranch_vccz .LBB0_1472
	s_add_i32 s3, s3, -8
	s_cmp_eq_u32 s3, 0
	s_cselect_b64 s[6:7], -1, 0
	s_sleep 2
